# nt hints plus relaxed vmcnt waits in GDN recurrence loop (loads of next-next chunk waited 1.5 steps later)
# speedup vs baseline: 1.0013x; 1.0013x over previous
.LBB0_1553:
	s_and_b64 vcc, exec, s[0:1]
	s_cbranch_vccz .LBB0_1544
	s_ashr_i32 s62, s51, 5
	s_bfe_u32 s6, s51, 0x30002
	s_lshl_b32 s0, s62, 10
	s_or_b32 s0, s0, s6
	s_ashr_i32 s1, s0, 31
	s_lshl_b64 s[60:61], s[0:1], 14
	v_mov_b32_e32 v22, 0
	v_lshl_add_u64 v[2:3], v[94:95], 0, s[60:61]
	s_barrier
	v_lshl_add_u64 v[4:5], v[96:97], 0, s[60:61]
	global_load_dwordx4 v[30:33], v[2:3], off
	global_load_dwordx4 v[34:37], v[4:5], off
	v_add_co_u32_e32 v2, vcc, s49, v2
	v_readfirstlane_b32 s5, v0
	v_lshl_add_u64 v[6:7], v[98:99], 0, s[60:61]
	v_addc_co_u32_e32 v3, vcc, 0, v3, vcc
	global_load_dwordx4 v[38:41], v[6:7], off
	global_load_dwordx4 v[42:45], v[2:3], off
	v_add_co_u32_e32 v2, vcc, s49, v4
	s_lshr_b32 s7, s5, 3
	s_lshr_b32 s5, s5, 2
	s_lshl_b64 s[18:19], s[0:1], 13
	v_addc_co_u32_e32 v3, vcc, 0, v5, vcc
	s_and_b32 s63, s7, 0x1ffffff0
	s_and_b32 s64, s5, 0x3ffffff0
	s_and_b32 s5, s5, 16
	v_add_co_u32_e32 v4, vcc, s49, v6
	s_add_u32 s7, s3, s60
	s_nop 0
	v_addc_co_u32_e32 v5, vcc, 0, v7, vcc
	global_load_dwordx4 v[46:49], v[2:3], off
	global_load_dwordx4 v[50:53], v[4:5], off
	v_lshl_add_u64 v[2:3], v[92:93], 0, s[18:19]
	s_addc_u32 s13, s20, s61
	s_lshl_b32 s18, s51, 6
	s_and_b32 s65, s18, 0xc0
	s_add_u32 s7, s7, s65
	s_addc_u32 s13, s13, 0
	s_lshl_b32 s66, s5, 1
	s_add_u32 s18, s7, s66
	s_addc_u32 s19, s13, 0
	v_lshlrev_b32_e32 v90, 1, v162
	v_lshl_add_u64 v[4:5], s[18:19], 0, v[90:91]
	s_lshl_b64 s[18:19], s[0:1], 2
	s_add_u32 s18, s10, s18
	v_or_b32_e32 v64, s63, v101
	v_ashrrev_i32_e32 v23, 31, v22
	s_addc_u32 s19, s11, s19
	s_or_b32 s0, s0, 8
	v_lshlrev_b32_e32 v58, 8, v64
	v_mov_b32_e32 v59, v91
	v_lshlrev_b64 v[60:61], 2, v[22:23]
	s_ashr_i32 s1, s0, 31
	v_lshl_add_u64 v[4:5], v[4:5], 0, v[58:59]
	global_load_dwordx4 v[54:57], v[2:3], off
	global_load_ushort v65, v[4:5], off
	global_load_ushort v66, v[4:5], off offset:256
	global_load_ushort v67, v[4:5], off offset:512
	global_load_ushort v68, v[4:5], off offset:768
	v_lshl_add_u64 v[2:3], s[18:19], 0, v[60:61]
	s_lshl_b64 s[18:19], s[0:1], 13
	s_lshl_b64 s[60:61], s[0:1], 14
	s_add_u32 s7, s3, s60
	v_lshl_add_u64 v[14:15], v[94:95], 0, s[60:61]
	s_addc_u32 s13, s20, s61
	global_load_dword v70, v[2:3], off
	s_nop 0
	global_load_dwordx4 v[2:5], v[14:15], off
	v_add_co_u32_e32 v14, vcc, s49, v14
	s_add_u32 s7, s7, s65
	v_lshl_add_u64 v[16:17], v[96:97], 0, s[60:61]
	v_addc_co_u32_e32 v15, vcc, 0, v15, vcc
	s_addc_u32 s13, s13, 0
	v_add_co_u32_e32 v18, vcc, s49, v16
	v_lshl_add_u64 v[26:27], v[92:93], 0, s[18:19]
	s_add_u32 s18, s7, s66
	v_lshl_add_u64 v[24:25], v[98:99], 0, s[60:61]
	v_addc_co_u32_e32 v19, vcc, 0, v17, vcc
	s_addc_u32 s19, s13, 0
	global_load_dwordx4 v[6:9], v[16:17], off
	global_load_dwordx4 v[10:13], v[24:25], off
	v_add_co_u32_e32 v24, vcc, s49, v24
	v_lshl_add_u64 v[62:63], s[18:19], 0, v[90:91]
	s_nop 0
	v_addc_co_u32_e32 v25, vcc, 0, v25, vcc
	v_lshl_add_u64 v[62:63], v[62:63], 0, v[58:59]
	v_lshl_add_u64 v[104:105], s[10:11], 0, v[60:61]
	global_load_dwordx4 v[14:17], v[14:15], off
	s_nop 0
	global_load_dwordx4 v[18:21], v[18:19], off
	v_add_u32_e32 v69, 0, v22
	global_load_dwordx4 v[22:25], v[24:25], off
	s_nop 0
	global_load_dwordx4 v[26:29], v[26:27], off
	v_lshl_add_u64 v[60:61], s[0:1], 2, v[104:105]
	global_load_ushort v158, v[62:63], off
	global_load_ushort v159, v[62:63], off offset:256
	global_load_ushort v160, v[62:63], off offset:512
	global_load_ushort v161, v[62:63], off offset:768
	global_load_dword v163, v[60:61], off
	v_add_u32_e32 v60, 0x1e800, v69
	v_or_b32_e32 v62, s64, v101
	v_add_u32_e32 v61, v60, v103
	v_lshlrev_b32_e32 v63, 1, v62
	s_lshl_b32 s7, s62, 7
	v_add_u32_e32 v133, v61, v63
	v_add_u32_e32 v61, v60, v116
	s_add_u32 s0, s3, s65
	s_mov_b32 s13, s12
	v_add_u32_e32 v134, v61, v63
	v_add_u32_e32 v61, v69, v117
	s_addc_u32 s1, s20, 0
	v_mov_b64_e32 v[72:73], s[12:13]
	v_add_u32_e32 v135, v61, v119
	s_add_u32 s0, s0, s66
	ds_write_b64 v133, v[72:73]
	ds_write_b64 v134, v[72:73]
	s_waitcnt vmcnt(23)
	ds_write_b128 v135, v[30:33]
	s_waitcnt vmcnt(22)
	ds_write_b128 v135, v[34:37] offset:17408
	v_add_u32_e32 v30, v69, v120
	s_addc_u32 s1, s1, 0
	v_add_u32_e32 v139, v30, v118
	v_lshl_add_u64 v[30:31], s[0:1], 0, v[90:91]
	v_or_b32_e32 v34, s63, v162
	s_movk_i32 s0, 0x110
	v_mul_lo_u32 v35, v34, s0
	s_lshl_b32 s0, s6, 8
	s_add_u32 s0, s21, s0
	v_add_u32_e32 v62, v69, v118
	s_addc_u32 s1, s22, 0
	v_add_u32_e32 v136, v62, v120
	v_add_u32_e32 v137, v61, v121
	v_add_u32_e32 v138, v62, v122
	s_add_u32 s0, s0, s65
	s_waitcnt vmcnt(21)
	ds_write_b128 v136, v[38:41] offset:44032
	s_waitcnt vmcnt(20)
	ds_write_b128 v137, v[42:45]
	s_waitcnt vmcnt(19)
	ds_write_b128 v137, v[46:49] offset:17408
	s_waitcnt vmcnt(18)
	ds_write_b128 v138, v[50:53] offset:44032
	v_or_b32_e32 v41, s64, v162
	s_addc_u32 s1, s1, 0
	v_add_u32_e32 v32, 0x20900, v69
	v_add_u32_e32 v33, 0x22a00, v69
	s_waitcnt vmcnt(17)
	ds_write_b128 v139, v[54:57] offset:34816
	s_waitcnt vmcnt(16)
	v_cvt_f32_f16_e32 v87, v65
	s_waitcnt vmcnt(15)
	v_cvt_f32_f16_e32 v88, v66
	s_waitcnt vmcnt(14)
	v_cvt_f32_f16_e32 v89, v67
	s_waitcnt vmcnt(13)
	v_cvt_f32_f16_e32 v157, v68
	s_waitcnt lgkmcnt(0)
	s_barrier
	v_or_b32_e32 v37, s5, v162
	v_mul_lo_u32 v34, v34, s24
	v_mul_lo_u32 v41, v41, s24
	s_add_u32 s0, s0, s66
	v_add_u32_e32 v46, 0x13800, v69
	v_add_u32_e32 v47, 0x1a000, v69
	v_add_u32_e32 v48, 0x17c00, v69
	v_add_u32_e32 v36, v69, v35
	v_mad_u32_u24 v38, v37, s23, v60
	v_mad_u32_u24 v140, v37, s25, v33
	v_lshlrev_b32_e32 v39, 1, v64
	v_add_u32_e32 v40, v69, v34
	v_add_u32_e32 v42, v69, v41
	v_add_u32_e32 v43, v33, v124
	v_add_u32_e32 v33, v33, v125
	s_addc_u32 s1, s1, 0
	v_add_u32_e32 v44, v32, v103
	v_add_u32_e32 v45, v32, v116
	v_add_u32_e32 v49, v48, v120
	v_mad_u32_u24 v32, v37, s23, v32
	v_add_u32_e32 v35, v46, v35
	v_add_u32_e32 v34, v48, v34
	v_add_u32_e32 v37, v47, v41
	v_mov_b32_e32 v62, 0
	s_mov_b32 s4, 0
	v_lshl_add_u32 v106, s62, 13, v64
	v_lshl_add_u64 v[108:109], s[0:1], 0, v[90:91]
	v_add_u32_e32 v90, v46, v117
	v_add_u32_e32 v141, v47, v118
	s_or_b32 s13, s7, 3
	v_lshl_add_u64 v[110:111], v[30:31], 0, v[58:59]
	v_add_u32_e32 v142, v36, v123
	v_add_u32_e32 v143, v38, v123
	v_add_u32_e32 v144, v140, v39
	v_add_u32_e32 v145, v40, v123
	v_add_u32_e32 v146, v42, v123
	v_add_u32_e32 v147, v43, v123
	v_add_u32_e32 v148, v33, v123
	v_add_u32_e32 v149, v44, v63
	v_add_u32_e32 v150, v45, v63
	v_add_u32_e32 v151, v49, v118
	v_add_u32_e32 v152, v32, v123
	v_add_u32_e32 v153, v35, v123
	v_add_u32_e32 v154, v34, v123
	v_add_u32_e32 v155, v37, v123
	v_mov_b32_e32 v63, v62
	v_mov_b32_e32 v64, v62
	v_mov_b32_e32 v65, v62
	v_mov_b32_e32 v66, v62
	v_mov_b32_e32 v67, v62
	v_mov_b32_e32 v68, v62
	v_mov_b32_e32 v69, v62
	s_waitcnt vmcnt(0)
.LBB0_1555:
	s_add_i32 s18, s4, 2
	v_ashrrev_i32_e32 v107, 31, v106
	s_cmpk_lt_u32 s4, 0x7e
	v_lshlrev_b64 v[72:73], 11, v[106:107]
	s_cselect_b64 s[0:1], -1, 0
	v_lshl_add_u64 v[242:243], v[108:109], 0, v[72:73]
	s_and_b64 vcc, s[0:1], exec
	v_add_co_u32_e64 v192, s[0:1], s50, v242
	ds_read2_b64 v[50:53], v142 offset1:4
	ds_read2_b64 v[30:33], v143 offset1:4
	ds_read2_b64 v[58:61], v142 offset0:8 offset1:12
	ds_read2_b64 v[34:37], v143 offset0:8 offset1:12
	ds_read2_b64 v[46:49], v142 offset0:16 offset1:20
	ds_read2_b64 v[38:41], v143 offset0:16 offset1:20
	ds_read2_b64 v[54:57], v142 offset0:24 offset1:28
	ds_read2_b64 v[42:45], v143 offset0:24 offset1:28
	v_addc_co_u32_e64 v193, s[0:1], 0, v243, s[0:1]
	s_cselect_b32 s0, s18, 0x7f
	s_min_u32 s1, s4, 0x7c
	s_add_i32 s0, s0, s7
	s_add_i32 s1, s13, s1
	s_lshl_b32 s0, s0, 3
	s_waitcnt lgkmcnt(6)
	v_mfma_f32_16x16x32_f16 v[78:81], v[50:53], v[30:33], 0
	s_lshl_b32 s1, s1, 3
	s_or_b32 s0, s0, s6
	s_or_b32 s60, s1, s6
	s_waitcnt lgkmcnt(4)
	v_mfma_f32_16x16x32_f16 v[178:181], v[58:61], v[34:37], 0
	s_ashr_i32 s1, s0, 31
	s_ashr_i32 s61, s60, 31
	s_lshl_b64 s[64:65], s[0:1], 14
	s_lshl_b64 s[62:63], s[0:1], 13
	v_lshl_add_u64 v[82:83], s[0:1], 2, v[104:105]
	s_lshl_b64 s[0:1], s[60:61], 13
	v_lshl_add_u64 v[50:51], v[94:95], 0, s[64:65]
	s_waitcnt lgkmcnt(2)
	v_mfma_f32_16x16x32_f16 v[182:185], v[46:49], v[38:41], v[78:81]
	v_lshl_add_u64 v[202:203], v[92:93], 0, s[0:1]
	v_add_co_u32_e64 v188, s[0:1], s49, v50
	s_waitcnt lgkmcnt(0)
	v_mfma_f32_16x16x32_f16 v[54:57], v[54:57], v[42:45], v[178:181]
	v_mul_f32_e64 v64, v64, v70
	v_mul_f32_e64 v65, v65, v70
	v_pk_mul_f32 v[62:63], v[62:63], v[70:71] op_sel_hi:[1,0]
	v_pk_mul_f32 v[68:69], v[68:69], v[70:71] op_sel_hi:[1,0]
	v_pk_mul_f32 v[66:67], v[66:67], v[70:71] op_sel_hi:[1,0]
	v_add_u32_e32 v70, 64, v106
	v_lshl_add_u64 v[52:53], v[96:97], 0, s[64:65]
	v_addc_co_u32_e64 v189, s[0:1], 0, v51, s[0:1]
	v_ashrrev_i32_e32 v71, 31, v70
	v_add_co_u32_e64 v190, s[0:1], s49, v52
	v_lshlrev_b64 v[70:71], 11, v[70:71]
	v_lshl_add_u64 v[84:85], v[98:99], 0, s[64:65]
	v_addc_co_u32_e64 v191, s[0:1], 0, v53, s[0:1]
	v_pk_add_f32 v[56:57], v[184:185], v[56:57]
	v_pk_add_f32 v[54:55], v[182:183], v[54:55]
	v_lshl_add_u64 v[112:113], v[108:109], 0, v[70:71]
	global_load_dwordx4 v[58:61], v[50:51], off
	global_load_dwordx4 v[70:73], v[52:53], off
	global_load_dwordx4 v[74:77], v[84:85], off
	v_add_co_u32_e64 v84, s[0:1], s49, v84
	v_sub_f32_e32 v57, v157, v57
	v_sub_f32_e32 v56, v89, v56
	v_sub_f32_e32 v55, v88, v55
	v_sub_f32_e32 v54, v87, v54
	v_lshl_add_u64 v[174:175], v[92:93], 0, s[62:63]
	v_lshl_add_u64 v[176:177], v[110:111], 0, s[64:65]
	v_addc_co_u32_e64 v85, s[0:1], 0, v85, s[0:1]
	v_cvt_pk_f16_f32 v54, v54, v55
	v_cvt_pk_f16_f32 v55, v56, v57
	v_add_u32_e32 v115, 0x4000, v142
	global_load_dwordx4 v[50:53], v[174:175], off
	global_load_ushort v173, v[176:177], off
	s_nop 0
	global_load_ushort v174, v[176:177], off offset:256
	global_load_ushort v175, v[176:177], off offset:512
	s_nop 0
	global_load_ushort v176, v[176:177], off offset:768
	s_nop 0
	global_load_dword v107, v[82:83], off
	global_load_dwordx4 v[46:49], v[188:189], off
	global_load_dwordx4 v[78:81], v[190:191], off
	s_nop 0
	global_load_dwordx4 v[82:85], v[84:85], off
	ds_write_b64 v144, v[54:55]
	ds_read2_b64 v[54:57], v115 offset0:128 offset1:132
	ds_read2_b64 v[178:181], v115 offset0:136 offset1:140
	ds_read2_b64 v[182:185], v115 offset0:144 offset1:148
	ds_read2_b64 v[188:191], v115 offset0:152 offset1:156
	v_add_u32_e32 v164, 0xa800, v146
	s_waitcnt lgkmcnt(0)
	s_barrier
	s_waitcnt lgkmcnt(3)
	v_mfma_f32_16x16x32_f16 v[30:33], v[54:57], v[30:33], 0
	ds_read2_b64 v[54:57], v164 offset0:128 offset1:132
	v_add_u32_e32 v240, 0x8800, v145
	v_add_u32_e32 v156, v140, v123
	s_waitcnt lgkmcnt(3)
	v_mfma_f32_16x16x32_f16 v[34:37], v[178:181], v[34:37], 0
	ds_read2_b64 v[178:181], v147 offset1:4
	v_add_u32_e32 v169, v90, v119
	v_add_u32_e32 v170, v141, v120
	s_waitcnt lgkmcnt(0)
	v_mfma_f32_16x16x32_f16 v[62:65], v[54:57], v[178:181], v[62:65]
	ds_read2_b64 v[178:181], v148 offset1:4
	v_add_u32_e32 v171, v90, v121
	v_add_u32_e32 v172, v141, v122
	v_mfma_f32_16x16x32_f16 v[30:33], v[182:185], v[38:41], v[30:33]
	ds_read2_b64 v[38:41], v164 offset0:136 offset1:140
	s_lshl_b64 s[66:67], s[60:61], 14
	v_lshl_add_u64 v[196:197], v[94:95], 0, s[66:67]
	s_waitcnt lgkmcnt(1)
	v_mfma_f32_16x16x32_f16 v[54:57], v[54:57], v[178:181], v[66:69]
	v_add_u32_e32 v244, 0xf000, v142
	v_add_co_u32_e64 v206, s[0:1], s49, v196
	v_mfma_f32_16x16x32_f16 v[34:37], v[188:191], v[42:45], v[34:37]
	ds_read2_b64 v[42:45], v147 offset0:8 offset1:12
	ds_read2_b64 v[66:69], v240 offset1:4
	v_lshl_add_u64 v[198:199], v[96:97], 0, s[66:67]
	v_addc_co_u32_e64 v207, s[0:1], 0, v197, s[0:1]
	s_waitcnt lgkmcnt(1)
	v_mfma_f32_16x16x32_f16 v[42:45], v[38:41], v[42:45], v[62:65]
	s_nop 2
	ds_read2_b64 v[62:65], v148 offset0:8 offset1:12
	ds_read2_b64 v[178:181], v156 offset1:4
	v_add_co_u32_e64 v208, s[0:1], s49, v198
	s_waitcnt lgkmcnt(1)
	v_mfma_f32_16x16x32_f16 v[38:41], v[38:41], v[62:65], v[54:57]
	ds_read2_b64 v[62:65], v156 offset0:8 offset1:12
	v_lshl_add_u64 v[200:201], v[98:99], 0, s[66:67]
	s_nop 0
	ds_read2_b64 v[54:57], v240 offset0:8 offset1:12
	s_waitcnt lgkmcnt(2)
	v_mfma_f32_16x16x32_f16 v[30:33], v[66:69], v[178:181], v[30:33]
	v_addc_co_u32_e64 v209, s[0:1], 0, v199, s[0:1]
	v_add_co_u32_e64 v88, s[0:1], s49, v200
	s_waitcnt lgkmcnt(0)
	v_mfma_f32_16x16x32_f16 v[34:37], v[54:57], v[62:65], v[34:37]
	v_cvt_pk_f16_f32 v63, v44, v45
	v_cvt_pk_f16_f32 v62, v42, v43
	v_cvt_pk_f16_f32 v65, v40, v41
	v_cvt_pk_f16_f32 v64, v38, v39
	ds_write_b64 v149, v[62:63]
	ds_write_b64 v150, v[64:65]
	s_waitcnt vmcnt(21)
	ds_write_b128 v135, v[2:5] offset:62464
	ds_write_b128 v169, v[6:9]
	ds_write_b128 v170, v[10:13]
	ds_write_b128 v137, v[14:17] offset:62464
	ds_write_b128 v171, v[18:21]
	ds_write_b128 v172, v[22:25]
	ds_write_b128 v151, v[26:29]
	v_add_f32_e32 v2, v30, v34
	v_add_f32_e32 v3, v31, v35
	v_cvt_f16_f32_e32 v2, v2
	v_add_f32_e32 v4, v32, v36
	v_cvt_f16_f32_e32 v3, v3
	v_add_f32_e32 v5, v33, v37
	v_cvt_f16_f32_e32 v4, v4
	v_cvt_f16_f32_e32 v5, v5
	global_store_short v[242:243], v2, off
	global_store_short v[242:243], v3, off offset:2048
	global_store_short v[192:193], v4, off
	global_store_short v[192:193], v5, off offset:2048
	s_waitcnt lgkmcnt(0)
	s_barrier
	global_load_dwordx4 v[2:5], v[196:197], off
	global_load_dwordx4 v[6:9], v[198:199], off
	ds_read2_b64 v[26:29], v244 offset0:128 offset1:132
	v_addc_co_u32_e64 v89, s[0:1], 0, v201, s[0:1]
	global_load_dwordx4 v[10:13], v[200:201], off
	global_load_dwordx4 v[14:17], v[206:207], off
	ds_read2_b64 v[62:65], v152 offset1:4
	ds_read2_b64 v[34:37], v244 offset0:136 offset1:140
	s_waitcnt vmcnt(20)
	v_mov_b32_e32 v86, v163
	v_pk_mul_f32 v[56:57], v[86:87], v[44:45] op_sel_hi:[0,1]
	v_pk_mul_f32 v[54:55], v[86:87], v[42:43] op_sel_hi:[0,1]
	v_pk_mul_f32 v[180:181], v[86:87], v[40:41] op_sel_hi:[0,1]
	v_pk_mul_f32 v[178:179], v[86:87], v[38:39] op_sel_hi:[0,1]
	global_load_dwordx4 v[18:21], v[208:209], off
	global_load_dwordx4 v[22:25], v[88:89], off
	ds_read2_b64 v[86:89], v152 offset0:8 offset1:12
	ds_read2_b64 v[38:41], v244 offset0:144 offset1:148
	v_lshl_add_u64 v[204:205], v[110:111], 0, s[66:67]
	v_cvt_f32_f16_e32 v166, v159
	v_cvt_f32_f16_e32 v165, v158
	v_cvt_f32_f16_e32 v167, v160
	v_cvt_f32_f16_e32 v168, v161
	v_lshl_add_u64 v[194:195], s[60:61], 2, v[104:105]
	s_waitcnt lgkmcnt(3)
	v_mfma_f32_16x16x32_f16 v[42:45], v[26:29], v[62:65], 0
	global_load_dwordx4 v[26:29], v[202:203], off
	ds_read2_b64 v[30:33], v152 offset0:16 offset1:20
	ds_read2_b64 v[66:69], v244 offset0:152 offset1:156
	global_load_ushort v158, v[204:205], off
	global_load_ushort v159, v[204:205], off offset:256
	s_waitcnt lgkmcnt(3)
	v_mfma_f32_16x16x32_f16 v[182:185], v[34:37], v[86:89], 0
	ds_read2_b64 v[34:37], v152 offset0:24 offset1:28
	global_load_ushort v160, v[204:205], off offset:512
	global_load_ushort v161, v[204:205], off offset:768
	global_load_dword v163, v[194:195], off
	v_add_co_u32_e64 v114, s[4:5], s50, v112
	s_waitcnt lgkmcnt(2)
	v_mfma_f32_16x16x32_f16 v[38:41], v[38:41], v[30:33], v[42:45]
	v_addc_co_u32_e64 v115, s[0:1], 0, v113, s[4:5]
	s_waitcnt vmcnt(20)
	v_cvt_f32_f16_e32 v157, v176
	s_waitcnt lgkmcnt(0)
	v_mfma_f32_16x16x32_f16 v[42:45], v[66:69], v[34:37], v[182:185]
	v_add_u32_e32 v106, 0x80, v106
	s_mov_b32 s4, s18
	s_nop 5
	v_add_f32_e32 v38, v38, v42
	v_add_f32_e32 v39, v39, v43
	v_add_f32_e32 v40, v40, v44
	v_add_f32_e32 v41, v41, v45
	v_sub_f32_e32 v38, v165, v38
	v_sub_f32_e32 v42, v166, v39
	v_sub_f32_e32 v39, v167, v40
	v_sub_f32_e32 v40, v168, v41
	v_cvt_pk_f16_f32 v39, v39, v40
	v_cvt_pk_f16_f32 v38, v38, v42
	ds_write_b64 v144, v[38:39]
	ds_read2_b64 v[66:69], v153 offset1:4
	ds_read2_b64 v[164:167], v153 offset0:8 offset1:12
	ds_read2_b64 v[42:45], v153 offset0:16 offset1:20
	ds_read2_b64 v[38:41], v153 offset0:24 offset1:28
	s_waitcnt lgkmcnt(0)
	s_barrier
	ds_read2_b64 v[168:171], v155 offset1:4
	s_waitcnt lgkmcnt(4)
	v_mfma_f32_16x16x32_f16 v[66:69], v[66:69], v[62:65], 0
	ds_read2_b64 v[62:65], v147 offset1:4
	s_waitcnt lgkmcnt(3)
	v_mfma_f32_16x16x32_f16 v[30:33], v[42:45], v[30:33], v[66:69]
	ds_read2_b64 v[42:45], v155 offset0:8 offset1:12
	v_mfma_f32_16x16x32_f16 v[86:89], v[164:167], v[86:89], 0
	s_waitcnt lgkmcnt(1)
	v_mfma_f32_16x16x32_f16 v[62:65], v[168:171], v[62:65], v[54:57]
	s_nop 2
	ds_read2_b64 v[54:57], v148 offset1:4
	v_mfma_f32_16x16x32_f16 v[34:37], v[38:41], v[34:37], v[86:89]
	ds_read2_b64 v[38:41], v147 offset0:8 offset1:12
	s_nop 1
	ds_read2_b64 v[86:89], v154 offset1:4
	s_waitcnt lgkmcnt(2)
	v_mfma_f32_16x16x32_f16 v[54:57], v[168:171], v[54:57], v[178:181]
	s_waitcnt lgkmcnt(1)
	v_mfma_f32_16x16x32_f16 v[62:65], v[42:45], v[38:41], v[62:65]
	ds_read2_b64 v[38:41], v148 offset0:8 offset1:12
	ds_read2_b64 v[164:167], v156 offset1:4
	s_waitcnt lgkmcnt(1)
	v_mfma_f32_16x16x32_f16 v[66:69], v[42:45], v[38:41], v[54:57]
	ds_read2_b64 v[38:41], v154 offset0:8 offset1:12
	ds_read2_b64 v[42:45], v156 offset0:8 offset1:12
	s_waitcnt lgkmcnt(2)
	v_mfma_f32_16x16x32_f16 v[30:33], v[86:89], v[164:167], v[30:33]
	v_cvt_f32_f16_e32 v87, v173
	v_cvt_f32_f16_e32 v88, v174
	v_cvt_f32_f16_e32 v89, v175
	s_waitcnt lgkmcnt(0)
	v_mfma_f32_16x16x32_f16 v[34:37], v[38:41], v[42:45], v[34:37]
	v_cvt_pk_f16_f32 v39, v64, v65
	v_cvt_pk_f16_f32 v38, v62, v63
	v_cvt_pk_f16_f32 v41, v68, v69
	s_nop 4
	v_add_f32_e32 v30, v30, v34
	v_add_f32_e32 v31, v31, v35
	v_cvt_f16_f32_e32 v30, v30
	v_add_f32_e32 v32, v32, v36
	v_cvt_f16_f32_e32 v31, v31
	v_add_f32_e32 v33, v33, v37
	v_cvt_f16_f32_e32 v32, v32
	v_cvt_f16_f32_e32 v33, v33
	v_cvt_pk_f16_f32 v40, v66, v67
	ds_write_b64 v133, v[38:39]
	ds_write_b64 v134, v[40:41]
	ds_write_b128 v135, v[58:61]
	ds_write_b128 v135, v[70:73] offset:17408
	ds_write_b128 v136, v[74:77] offset:44032
	s_waitcnt vmcnt(18)
	ds_write_b128 v137, v[46:49]
	s_waitcnt vmcnt(17)
	ds_write_b128 v137, v[78:81] offset:17408
	s_waitcnt vmcnt(16)
	ds_write_b128 v138, v[82:85] offset:44032
	ds_write_b128 v139, v[50:53] offset:34816
	global_store_short v[112:113], v30, off
	global_store_short v[112:113], v31, off offset:2048
	global_store_short v[114:115], v32, off
	global_store_short v[114:115], v33, off offset:2048
	s_waitcnt lgkmcnt(0)
	s_barrier
	v_mov_b32_e32 v70, v107
	s_cbranch_vccnz .LBB0_1555
	s_waitcnt vmcnt(0)
	s_waitcnt lgkmcnt(0)
	s_barrier
	s_branch .LBB0_1544

	.amdhsa_kernel _Z10hybrid_fwd4Args
		.amdhsa_group_segment_fixed_size 0
		.amdhsa_private_segment_fixed_size 0
		.amdhsa_kernarg_size 552
		.amdhsa_user_sgpr_count 2
		.amdhsa_user_sgpr_dispatch_ptr 0
		.amdhsa_user_sgpr_queue_ptr 0
		.amdhsa_user_sgpr_kernarg_segment_ptr 1
		.amdhsa_user_sgpr_dispatch_id 0
		.amdhsa_user_sgpr_kernarg_preload_length 0
		.amdhsa_user_sgpr_kernarg_preload_offset 0
		.amdhsa_user_sgpr_private_segment_size 0
		.amdhsa_uses_dynamic_stack 0
		.amdhsa_enable_private_segment 0
		.amdhsa_system_sgpr_workgroup_id_x 1
		.amdhsa_system_sgpr_workgroup_id_y 0
		.amdhsa_system_sgpr_workgroup_id_z 0
		.amdhsa_system_sgpr_workgroup_info 0
		.amdhsa_system_vgpr_workitem_id 0
		.amdhsa_next_free_vgpr 248
		.amdhsa_next_free_sgpr 98
		.amdhsa_accum_offset 248
		.amdhsa_reserve_vcc 1
		.amdhsa_float_round_mode_32 0
		.amdhsa_float_round_mode_16_64 0
		.amdhsa_float_denorm_mode_32 3
		.amdhsa_float_denorm_mode_16_64 3
		.amdhsa_dx10_clamp 1
		.amdhsa_ieee_mode 1
		.amdhsa_fp16_overflow 0
		.amdhsa_tg_split 0
		.amdhsa_exception_fp_ieee_invalid_op 0
		.amdhsa_exception_fp_denorm_src 0
		.amdhsa_exception_fp_ieee_div_zero 0
		.amdhsa_exception_fp_ieee_overflow 0
		.amdhsa_exception_fp_ieee_underflow 0
		.amdhsa_exception_fp_ieee_inexact 0
		.amdhsa_exception_int_div_zero 0
	.end_amdhsa_kernel

amdhsa.kernels:
  - .agpr_count:     0
    .args:
      - .offset:         0
        .size:           296
        .value_kind:     by_value
      - .offset:         296
        .size:           4
        .value_kind:     hidden_block_count_x
      - .offset:         300
        .size:           4
        .value_kind:     hidden_block_count_y
      - .offset:         304
        .size:           4
        .value_kind:     hidden_block_count_z
      - .offset:         308
        .size:           2
        .value_kind:     hidden_group_size_x
      - .offset:         310
        .size:           2
        .value_kind:     hidden_group_size_y
      - .offset:         312
        .size:           2
        .value_kind:     hidden_group_size_z
      - .offset:         314
        .size:           2
        .value_kind:     hidden_remainder_x
      - .offset:         316
        .size:           2
        .value_kind:     hidden_remainder_y
      - .offset:         318
        .size:           2
        .value_kind:     hidden_remainder_z
      - .offset:         336
        .size:           8
        .value_kind:     hidden_global_offset_x
      - .offset:         344
        .size:           8
        .value_kind:     hidden_global_offset_y
      - .offset:         352
        .size:           8
        .value_kind:     hidden_global_offset_z
      - .offset:         360
        .size:           2
        .value_kind:     hidden_grid_dims
      - .offset:         416
        .size:           4
        .value_kind:     hidden_dynamic_lds_size
    .group_segment_fixed_size: 0
    .kernarg_segment_align: 8
    .kernarg_segment_size: 552
    .language:       OpenCL C
    .language_version:
      - 2
      - 0
    .max_flat_workgroup_size: 512
    .name:           _Z10hybrid_fwd4Args
    .private_segment_fixed_size: 0
    .sgpr_count:     104
    .sgpr_spill_count: 89
    .symbol:         _Z10hybrid_fwd4Args.kd
    .uniform_work_group_size: 1
    .uses_dynamic_stack: false
    .vgpr_count:     248
    .vgpr_spill_count: 0
    .wavefront_size: 64
